# baseline (speedup 1.0000x reference)
_Z14k_scatter_nodePKiS0_PjPiPKfS4_PfS5_PDF16_:
	s_mov_b32 s31, s2
	s_mov_b64 s[34:35], s[0:1]
	s_cmpk_gt_i32 s2, 0xff
	s_mov_b64 s[4:5], -1
	s_cbranch_scc0 .LBB1_4
	s_load_dwordx8 s[12:19], s[34:35], 0x20
	s_load_dwordx2 s[20:21], s[34:35], 0x40
	v_lshrrev_b32_e32 v1, 6, v0
	v_and_b32_e32 v3, 15, v0
	v_bfe_u32 v4, v0, 4, 2
	s_lshl_b32 s3, s31, 8
	s_add_i32 s3, s3, 0xffff0000
	v_lshl_add_u32 v5, v1, 5, s3
	v_add_u32_e32 v6, v5, v3
	v_readfirstlane_b32 s22, v5
	v_add_u32_e32 v7, 16, v6
	s_mov_b32 s23, 0xc350
	s_cmp_ge_i32 s22, s23
	s_cbranch_scc1 .Lk2n_end
	v_min_i32_e32 v8, 0xc34f, v6
	v_min_i32_e32 v9, 0xc34f, v7
	v_lshlrev_b32_e32 v10, 4, v4
	v_lshl_add_u32 v8, v8, 8, v10
	v_lshl_add_u32 v9, v9, 8, v10
	v_lshlrev_b32_e32 v11, 2, v3
	v_lshl_add_u32 v11, v4, 8, v11
	s_waitcnt lgkmcnt(0)
	global_load_dwordx4 v[32:35], v8, s[12:13] nt
	global_load_dwordx4 v[36:39], v8, s[12:13] offset:64 nt
	global_load_dwordx4 v[40:43], v8, s[12:13] offset:128 nt
	global_load_dwordx4 v[44:47], v8, s[12:13] offset:192 nt
	global_load_dwordx4 v[48:51], v9, s[12:13] nt
	global_load_dwordx4 v[52:55], v9, s[12:13] offset:64 nt
	global_load_dwordx4 v[56:59], v9, s[12:13] offset:128 nt
	global_load_dwordx4 v[60:63], v9, s[12:13] offset:192 nt
	global_load_dword v16, v11, s[14:15]
	global_load_dword v17, v11, s[14:15] offset:64
	global_load_dword v18, v11, s[14:15] offset:128
	global_load_dword v19, v11, s[14:15] offset:192
	global_load_dword v20, v11, s[14:15] offset:1024
	global_load_dword v21, v11, s[14:15] offset:1088
	global_load_dword v22, v11, s[14:15] offset:1152
	global_load_dword v23, v11, s[14:15] offset:1216
	global_load_dword v24, v11, s[14:15] offset:2048
	global_load_dword v25, v11, s[14:15] offset:2112
	global_load_dword v26, v11, s[14:15] offset:2176
	global_load_dword v27, v11, s[14:15] offset:2240
	global_load_dword v28, v11, s[14:15] offset:3072
	global_load_dword v29, v11, s[14:15] offset:3136
	global_load_dword v30, v11, s[14:15] offset:3200
	global_load_dword v31, v11, s[14:15] offset:3264
	v_cmp_gt_i32_e64 s[24:25], s23, v6
	v_cmp_gt_i32_e64 s[26:27], s23, v7
	v_cmp_gt_u32_e32 vcc, 2, v4
	v_mov_b32_e32 v12, s18
	v_mov_b32_e32 v13, s19
	v_mov_b32_e32 v14, s16
	v_mov_b32_e32 v15, s17
	v_cndmask_b32_e32 v12, v12, v14, vcc
	v_cndmask_b32_e32 v13, v13, v15, vcc
	v_and_b32_e32 v14, 1, v4
	v_lshlrev_b32_e32 v14, 4, v14
	v_mov_b32_e32 v15, 0
	v_lshl_add_u32 v88, v6, 5, v14
	v_mov_b32_e32 v89, 0
	v_lshl_add_u32 v14, v7, 5, v14
	v_lshl_add_u64 v[88:89], v[88:89], 0, v[12:13]
	v_lshl_add_u64 v[90:91], v[14:15], 0, v[12:13]
	v_lshlrev_b32_e32 v10, 3, v4
	v_lshl_add_u32 v92, v6, 7, v10
	v_lshl_add_u32 v93, v7, 7, v10
	s_waitcnt vmcnt(0)
	v_mfma_f32_16x16x4_f32 v[64:67], v16, v32, 0
	v_mfma_f32_16x16x4_f32 v[68:71], v16, v48, 0
	v_mfma_f32_16x16x4_f32 v[64:67], v17, v33, v[64:67]
	v_mfma_f32_16x16x4_f32 v[68:71], v17, v49, v[68:71]
	v_mfma_f32_16x16x4_f32 v[64:67], v18, v34, v[64:67]
	v_mfma_f32_16x16x4_f32 v[68:71], v18, v50, v[68:71]
	v_mfma_f32_16x16x4_f32 v[64:67], v19, v35, v[64:67]
	v_mfma_f32_16x16x4_f32 v[68:71], v19, v51, v[68:71]
	v_mfma_f32_16x16x4_f32 v[64:67], v20, v36, v[64:67]
	v_mfma_f32_16x16x4_f32 v[68:71], v20, v52, v[68:71]
	v_mfma_f32_16x16x4_f32 v[64:67], v21, v37, v[64:67]
	v_mfma_f32_16x16x4_f32 v[68:71], v21, v53, v[68:71]
	v_mfma_f32_16x16x4_f32 v[64:67], v22, v38, v[64:67]
	v_mfma_f32_16x16x4_f32 v[68:71], v22, v54, v[68:71]
	v_mfma_f32_16x16x4_f32 v[64:67], v23, v39, v[64:67]
	v_mfma_f32_16x16x4_f32 v[68:71], v23, v55, v[68:71]
	v_mfma_f32_16x16x4_f32 v[64:67], v24, v40, v[64:67]
	v_mfma_f32_16x16x4_f32 v[68:71], v24, v56, v[68:71]
	v_mfma_f32_16x16x4_f32 v[64:67], v25, v41, v[64:67]
	v_mfma_f32_16x16x4_f32 v[68:71], v25, v57, v[68:71]
	v_mfma_f32_16x16x4_f32 v[64:67], v26, v42, v[64:67]
	v_mfma_f32_16x16x4_f32 v[68:71], v26, v58, v[68:71]
	v_mfma_f32_16x16x4_f32 v[64:67], v27, v43, v[64:67]
	v_mfma_f32_16x16x4_f32 v[68:71], v27, v59, v[68:71]
	v_mfma_f32_16x16x4_f32 v[64:67], v28, v44, v[64:67]
	v_mfma_f32_16x16x4_f32 v[68:71], v28, v60, v[68:71]
	v_mfma_f32_16x16x4_f32 v[64:67], v29, v45, v[64:67]
	v_mfma_f32_16x16x4_f32 v[68:71], v29, v61, v[68:71]
	v_mfma_f32_16x16x4_f32 v[64:67], v30, v46, v[64:67]
	v_mfma_f32_16x16x4_f32 v[68:71], v30, v62, v[68:71]
	v_mfma_f32_16x16x4_f32 v[64:67], v31, v47, v[64:67]
	v_mfma_f32_16x16x4_f32 v[68:71], v31, v63, v[68:71]
	v_cvt_pk_f16_f32 v72, v32, v33
	v_cvt_pk_f16_f32 v73, v34, v35
	v_cvt_pk_f16_f32 v74, v36, v37
	v_cvt_pk_f16_f32 v75, v38, v39
	v_cvt_pk_f16_f32 v76, v40, v41
	v_cvt_pk_f16_f32 v77, v42, v43
	v_cvt_pk_f16_f32 v78, v44, v45
	v_cvt_pk_f16_f32 v79, v46, v47
	v_cvt_pk_f16_f32 v80, v48, v49
	v_cvt_pk_f16_f32 v81, v50, v51
	v_cvt_pk_f16_f32 v82, v52, v53
	v_cvt_pk_f16_f32 v83, v54, v55
	v_cvt_pk_f16_f32 v84, v56, v57
	v_cvt_pk_f16_f32 v85, v58, v59
	v_cvt_pk_f16_f32 v86, v60, v61
	v_cvt_pk_f16_f32 v87, v62, v63
	s_mov_b64 exec, s[24:25]
	global_store_dwordx2 v92, v[72:73], s[20:21]
	global_store_dwordx2 v92, v[74:75], s[20:21] offset:32
	global_store_dwordx2 v92, v[76:77], s[20:21] offset:64
	global_store_dwordx2 v92, v[78:79], s[20:21] offset:96
	global_store_dwordx4 v[88:89], v[64:67], off nt
	s_mov_b64 exec, s[26:27]
	global_store_dwordx2 v93, v[80:81], s[20:21]
	global_store_dwordx2 v93, v[82:83], s[20:21] offset:32
	global_store_dwordx2 v93, v[84:85], s[20:21] offset:64
	global_store_dwordx2 v93, v[86:87], s[20:21] offset:96
	global_store_dwordx4 v[90:91], v[68:71], off nt
